# P10 output stores nt
# speedup vs baseline: 1.0378x; 1.0378x over previous
.LBB0_1224:
	s_add_i32 s2, s6, 1
	v_mov_b32_e32 v50, s6
	s_waitcnt vmcnt(2)
	v_cvt_pk_f32_fp8_e32 v[134:135], v6
	v_cvt_pk_f32_fp8_sdwa v[136:137], v6 src0_sel:WORD_1
	v_mov_b32_e32 v6, s2
	v_cmp_lt_i32_e32 vcc, s2, v46
	v_and_or_b32 v49, s6, 63, v33
	s_waitcnt vmcnt(1)
	v_lshlrev_b32_e32 v118, 16, v12
	v_cndmask_b32_e32 v6, v50, v6, vcc
	v_and_b32_e32 v119, 0xffff0000, v12
	v_lshlrev_b32_e32 v120, 16, v13
	v_and_b32_e32 v121, 0xffff0000, v13
	v_mad_u64_u32 v[12:13], s[6:7], v6, s3, v[32:33]
	v_and_or_b32 v6, v6, 63, v33
	v_lshlrev_b32_e32 v6, 2, v6
	v_cvt_pk_f32_fp8_e32 v[66:67], v24
	v_cvt_pk_f32_fp8_sdwa v[68:69], v24 src0_sel:WORD_1
	v_cvt_pk_f32_fp8_e32 v[90:91], v26
	v_cvt_pk_f32_fp8_sdwa v[92:93], v26 src0_sel:WORD_1
	ds_bpermute_b32 v24, v6, v47
	ds_bpermute_b32 v26, v6, v48
	v_ashrrev_i32_e32 v13, 31, v12
	v_cvt_pk_f32_fp8_e32 v[78:79], v25
	v_cvt_pk_f32_fp8_sdwa v[80:81], v25 src0_sel:WORD_1
	v_cvt_pk_f32_fp8_e32 v[102:103], v27
	v_cvt_pk_f32_fp8_sdwa v[104:105], v27 src0_sel:WORD_1
	v_lshlrev_b64 v[12:13], 12, v[12:13]
	s_waitcnt lgkmcnt(1)
	v_ashrrev_i32_e32 v25, 31, v24
	s_waitcnt lgkmcnt(0)
	v_ashrrev_i32_e32 v27, 31, v26
	v_lshl_add_u64 v[50:51], v[40:41], 0, v[12:13]
	v_lshlrev_b64 v[24:25], 11, v[24:25]
	v_lshlrev_b64 v[26:27], 11, v[26:27]
	v_cvt_pk_f32_fp8_e32 v[62:63], v20
	v_cvt_pk_f32_fp8_sdwa v[64:65], v20 src0_sel:WORD_1
	v_lshlrev_b32_e32 v70, 16, v28
	v_and_b32_e32 v71, 0xffff0000, v28
	v_lshlrev_b32_e32 v72, 16, v29
	v_and_b32_e32 v73, 0xffff0000, v29
	v_cvt_pk_f32_fp8_e32 v[74:75], v21
	v_cvt_pk_f32_fp8_sdwa v[76:77], v21 src0_sel:WORD_1
	v_lshlrev_b32_e32 v82, 16, v30
	v_and_b32_e32 v83, 0xffff0000, v30
	v_lshlrev_b32_e32 v84, 16, v31
	v_and_b32_e32 v85, 0xffff0000, v31
	v_cvt_pk_f32_fp8_e32 v[86:87], v22
	v_cvt_pk_f32_fp8_sdwa v[88:89], v22 src0_sel:WORD_1
	v_lshlrev_b32_e32 v94, 16, v16
	v_and_b32_e32 v95, 0xffff0000, v16
	v_lshlrev_b32_e32 v96, 16, v17
	v_and_b32_e32 v97, 0xffff0000, v17
	v_cvt_pk_f32_fp8_e32 v[98:99], v23
	v_cvt_pk_f32_fp8_sdwa v[100:101], v23 src0_sel:WORD_1
	v_lshlrev_b32_e32 v106, 16, v18
	v_and_b32_e32 v107, 0xffff0000, v18
	v_lshlrev_b32_e32 v108, 16, v19
	v_and_b32_e32 v109, 0xffff0000, v19
	v_cvt_pk_f32_fp8_e32 v[114:115], v4
	v_cvt_pk_f32_fp8_sdwa v[116:117], v4 src0_sel:WORD_1
	v_cvt_pk_f32_fp8_e32 v[124:125], v5
	v_cvt_pk_f32_fp8_sdwa v[126:127], v5 src0_sel:WORD_1
	v_lshlrev_b32_e32 v4, 16, v14
	v_and_b32_e32 v5, 0xffff0000, v14
	v_lshlrev_b32_e32 v128, 16, v15
	v_and_b32_e32 v129, 0xffff0000, v15
	global_load_dwordx4 v[28:31], v[50:51], off
	global_load_dwordx4 v[16:19], v[50:51], off offset:16
	global_load_dwordx4 v[12:15], v[50:51], off offset:2048
	global_load_dwordx4 v[20:23], v[50:51], off offset:2064
	v_lshl_add_u64 v[58:59], v[38:39], 0, v[24:25]
	v_lshl_add_u64 v[50:51], v[38:39], 0, v[26:27]
	global_load_dwordx4 v[24:27], v[50:51], off
	s_nop 0
	global_load_dwordx4 v[50:53], v[50:51], off offset:1024
	s_nop 0
	global_load_dwordx4 v[54:57], v[58:59], off
	s_nop 0
	global_load_dwordx4 v[58:61], v[58:59], off offset:1024
	v_lshlrev_b32_e32 v49, 2, v49
	ds_bpermute_b32 v148, v49, v34
	ds_bpermute_b32 v150, v49, v35
	v_cvt_pk_f32_fp8_e32 v[110:111], v8
	v_cvt_pk_f32_fp8_sdwa v[112:113], v8 src0_sel:WORD_1
	v_cvt_pk_f32_fp8_e32 v[122:123], v9
	v_cvt_pk_f32_fp8_sdwa v[8:9], v9 src0_sel:WORD_1
	v_cvt_pk_f32_fp8_e32 v[130:131], v10
	v_cvt_pk_f32_fp8_sdwa v[132:133], v10 src0_sel:WORD_1
	v_cvt_pk_f32_fp8_e32 v[140:141], v11
	v_cvt_pk_f32_fp8_sdwa v[10:11], v11 src0_sel:WORD_1
	v_ashrrev_i32_e32 v45, 31, v44
	v_cvt_pk_f32_fp8_e32 v[142:143], v7
	v_cvt_pk_f32_fp8_sdwa v[144:145], v7 src0_sel:WORD_1
	v_lshlrev_b64 v[146:147], 13, v[44:45]
	s_waitcnt vmcnt(8)
	v_lshlrev_b32_e32 v138, 16, v0
	v_and_b32_e32 v139, 0xffff0000, v0
	v_lshlrev_b32_e32 v0, 16, v1
	v_and_b32_e32 v1, 0xffff0000, v1
	v_lshlrev_b32_e32 v6, 16, v2
	v_and_b32_e32 v7, 0xffff0000, v2
	v_lshlrev_b32_e32 v2, 16, v3
	v_and_b32_e32 v3, 0xffff0000, v3
	v_lshl_add_u64 v[146:147], s[4:5], 0, v[146:147]
	s_waitcnt lgkmcnt(1)
	v_pk_fma_f32 v[62:63], v[62:63], v[148:149], v[70:71] op_sel_hi:[1,0,1]
	v_pk_fma_f32 v[64:65], v[64:65], v[148:149], v[72:73] op_sel_hi:[1,0,1]
	v_pk_fma_f32 v[70:71], v[74:75], v[148:149], v[82:83] op_sel_hi:[1,0,1]
	v_pk_fma_f32 v[72:73], v[76:77], v[148:149], v[84:85] op_sel_hi:[1,0,1]
	v_pk_fma_f32 v[74:75], v[86:87], v[148:149], v[94:95] op_sel_hi:[1,0,1]
	v_pk_fma_f32 v[76:77], v[88:89], v[148:149], v[96:97] op_sel_hi:[1,0,1]
	v_mov_b32_e32 v43, v37
	v_lshl_add_u64 v[152:153], v[146:147], 0, v[36:37]
	v_pk_fma_f32 v[82:83], v[98:99], v[148:149], v[106:107] op_sel_hi:[1,0,1]
	v_pk_fma_f32 v[84:85], v[100:101], v[148:149], v[108:109] op_sel_hi:[1,0,1]
	v_pk_fma_f32 v[86:87], v[110:111], v[148:149], v[118:119] op_sel_hi:[1,0,1]
	v_pk_fma_f32 v[88:89], v[112:113], v[148:149], v[120:121] op_sel_hi:[1,0,1]
	v_pk_fma_f32 v[94:95], v[122:123], v[148:149], v[4:5] op_sel_hi:[1,0,1]
	v_pk_fma_f32 v[96:97], v[8:9], v[148:149], v[128:129] op_sel_hi:[1,0,1]
	v_pk_fma_f32 v[98:99], v[130:131], v[148:149], v[138:139] op_sel_hi:[1,0,1]
	v_pk_fma_f32 v[100:101], v[132:133], v[148:149], v[0:1] op_sel_hi:[1,0,1]
	v_pk_fma_f32 v[106:107], v[140:141], v[148:149], v[6:7] op_sel_hi:[1,0,1]
	v_pk_fma_f32 v[108:109], v[10:11], v[148:149], v[2:3] op_sel_hi:[1,0,1]
	s_waitcnt lgkmcnt(0)
	v_pk_fma_f32 v[0:1], v[66:67], v[150:151], v[62:63] op_sel_hi:[1,0,1]
	v_pk_fma_f32 v[2:3], v[68:69], v[150:151], v[64:65] op_sel_hi:[1,0,1]
	v_pk_fma_f32 v[4:5], v[78:79], v[150:151], v[70:71] op_sel_hi:[1,0,1]
	v_pk_fma_f32 v[6:7], v[80:81], v[150:151], v[72:73] op_sel_hi:[1,0,1]
	v_pk_fma_f32 v[8:9], v[90:91], v[150:151], v[74:75] op_sel_hi:[1,0,1]
	v_pk_fma_f32 v[10:11], v[92:93], v[150:151], v[76:77] op_sel_hi:[1,0,1]
	v_cmp_eq_u32_e32 vcc, s2, v46
	v_lshl_add_u64 v[146:147], v[146:147], 0, v[42:43]
	v_pk_fma_f32 v[62:63], v[102:103], v[150:151], v[82:83] op_sel_hi:[1,0,1]
	v_pk_fma_f32 v[64:65], v[104:105], v[150:151], v[84:85] op_sel_hi:[1,0,1]
	v_pk_fma_f32 v[66:67], v[114:115], v[150:151], v[86:87] op_sel_hi:[1,0,1]
	v_pk_fma_f32 v[68:69], v[116:117], v[150:151], v[88:89] op_sel_hi:[1,0,1]
	v_pk_fma_f32 v[70:71], v[124:125], v[150:151], v[94:95] op_sel_hi:[1,0,1]
	v_pk_fma_f32 v[72:73], v[126:127], v[150:151], v[96:97] op_sel_hi:[1,0,1]
	v_pk_fma_f32 v[74:75], v[134:135], v[150:151], v[98:99] op_sel_hi:[1,0,1]
	v_pk_fma_f32 v[76:77], v[136:137], v[150:151], v[100:101] op_sel_hi:[1,0,1]
	v_pk_fma_f32 v[78:79], v[142:143], v[150:151], v[106:107] op_sel_hi:[1,0,1]
	v_pk_fma_f32 v[80:81], v[144:145], v[150:151], v[108:109] op_sel_hi:[1,0,1]
	global_store_dwordx4 v[152:153], v[0:3], off nt
	global_store_dwordx4 v[152:153], v[4:7], off offset:16 nt
	global_store_dwordx4 v[152:153], v[8:11], off offset:32 nt
	global_store_dwordx4 v[152:153], v[62:65], off offset:48 nt
	global_store_dwordx4 v[146:147], v[66:69], off nt
	global_store_dwordx4 v[146:147], v[70:73], off offset:16 nt
	global_store_dwordx4 v[146:147], v[74:77], off offset:32 nt
	global_store_dwordx4 v[146:147], v[78:81], off offset:48 nt
	v_add_u32_e32 v44, s3, v44
	s_mov_b32 s6, s2
	s_or_b64 s[0:1], vcc, s[0:1]
	s_waitcnt vmcnt(12)
	v_mov_b32_e32 v0, v20
	v_mov_b32_e32 v1, v21
	v_mov_b32_e32 v2, v22
	v_mov_b32_e32 v3, v23
	s_waitcnt vmcnt(10)
	v_mov_b64_e32 v[4:5], v[50:51]
	s_waitcnt vmcnt(9)
	v_mov_b64_e32 v[20:21], v[54:55]
	s_waitcnt vmcnt(8)
	v_mov_b64_e32 v[8:9], v[58:59]
	v_mov_b64_e32 v[6:7], v[52:53]
	v_mov_b64_e32 v[22:23], v[56:57]
	v_mov_b64_e32 v[10:11], v[60:61]
	s_andn2_b64 exec, exec, s[0:1]
	s_cbranch_execnz .LBB0_1224
